# same as the previous best plus a per-chunk fallback of the branch-combine loop for grids other than 256 workgroups
# speedup vs baseline: 1.0138x; 1.0108x over previous
.LBB0_1057:
	s_cmp_gt_i32 s72, 5
	s_cselect_b64 s[0:1], -1, 0
	s_cmp_lt_i32 s73, 6
	s_cselect_b64 s[2:3], -1, 0
	s_or_b64 s[0:1], s[0:1], s[2:3]
	s_and_b64 vcc, exec, s[0:1]
	s_cbranch_vccnz .LBB0_1111
	s_waitcnt vmcnt(0)
	v_mov_b32_e32 v2, v254
	s_mov_b32 s0, 0x400000
	v_lshl_add_u32 v1, s82, 9, v2
	v_cmp_gt_i32_e32 vcc, s0, v1
	s_and_saveexec_b64 s[4:5], vcc
	s_cbranch_execz .LBB0_1061
	s_add_u32 s6, s86, 0x45800000
	s_addc_u32 s7, s87, 0
	s_add_u32 s8, s86, 0x31800000
	s_addc_u32 s9, s87, 0
	s_add_u32 s10, s86, 0x7000000
	s_addc_u32 s11, s87, 0
	s_add_u32 s12, s86, 0xb000000
	v_lshlrev_b32_e32 v0, 3, v2
	s_addc_u32 s13, s87, 0
	s_lshl_b32 s18, s88, 9
	v_lshl_add_u32 v4, s82, 12, v0
	s_lshl_b32 s19, s88, 12
	s_mov_b64 s[14:15], 0
	v_mov_b32_e32 v3, 0
	v_mov_b32_e32 v43, 0
	v_mov_b32_e32 v83, 0
	v_mov_b32_e32 v123, 0
	s_mov_b64 s[16:17], 0xf008840
	s_mov_b32 s20, 0xf008000
	s_mov_b32 s21, 0xffff0000
	s_movk_i32 s22, 0x7fff
	s_mov_b32 s23, 0x3fffff
	s_cmpk_lg_i32 s88, 0x100
	s_cbranch_scc1 .Lcomb_orig
.LBB0_1060:
	v_ashrrev_i32_e32 v6, 8, v1
	v_bfe_u32 v2, v4, 7, 4
	v_mul_hi_i32_i24_e32 v9, 0x8a00, v6
	v_mul_i32_i24_e32 v8, 0x8a00, v6
	v_mul_u32_u24_e32 v2, 3, v2
	v_ashrrev_i32_e32 v7, 31, v6
	v_lshl_add_u64 v[8:9], s[86:87], 0, v[8:9]
	v_lshlrev_b32_e32 v2, 1, v2
	v_lshlrev_b64 v[18:19], 12, v[6:7]
	v_lshl_add_u64 v[6:7], v[8:9], 0, v[2:3]
	v_and_b32_e32 v0, 0x7f8, v4
	v_add_co_u32_e32 v22, vcc, s20, v6
	v_lshl_or_b32 v18, v0, 1, v18
	s_nop 0
	v_addc_co_u32_e32 v23, vcc, 0, v7, vcc
	v_lshl_add_u64 v[20:21], v[6:7], 0, s[16:17]
	v_lshl_add_u64 v[24:25], s[6:7], 0, v[18:19]
	v_lshl_add_u64 v[26:27], s[8:9], 0, v[18:19]
	v_lshl_add_u64 v[28:29], s[10:11], 0, v[18:19]
	global_load_dword v0, v[22:23], off offset:2112
	global_load_dwordx4 v[6:9], v[24:25], off
	global_load_ushort v2, v[20:21], off offset:4
	global_load_dwordx4 v[10:13], v[26:27], off
	global_load_dwordx4 v[14:17], v[28:29], off
	v_add_u32_e32 v1, s18, v1
	v_add_u32_e32 v4, s19, v4
	v_ashrrev_i32_e32 v46, 8, v1
	v_bfe_u32 v42, v4, 7, 4
	v_mul_hi_i32_i24_e32 v49, 0x8a00, v46
	v_mul_i32_i24_e32 v48, 0x8a00, v46
	v_mul_u32_u24_e32 v42, 3, v42
	v_ashrrev_i32_e32 v47, 31, v46
	v_lshl_add_u64 v[48:49], s[86:87], 0, v[48:49]
	v_lshlrev_b32_e32 v42, 1, v42
	v_lshlrev_b64 v[58:59], 12, v[46:47]
	v_lshl_add_u64 v[46:47], v[48:49], 0, v[42:43]
	v_and_b32_e32 v40, 0x7f8, v4
	v_add_co_u32_e32 v62, vcc, s20, v46
	v_lshl_or_b32 v58, v40, 1, v58
	s_nop 0
	v_addc_co_u32_e32 v63, vcc, 0, v47, vcc
	v_lshl_add_u64 v[60:61], v[46:47], 0, s[16:17]
	v_lshl_add_u64 v[64:65], s[6:7], 0, v[58:59]
	v_lshl_add_u64 v[66:67], s[8:9], 0, v[58:59]
	v_lshl_add_u64 v[68:69], s[10:11], 0, v[58:59]
	global_load_dword v40, v[62:63], off offset:2112
	global_load_dwordx4 v[46:49], v[64:65], off
	global_load_ushort v42, v[60:61], off offset:4
	global_load_dwordx4 v[50:53], v[66:67], off
	global_load_dwordx4 v[54:57], v[68:69], off
	v_add_u32_e32 v1, s18, v1
	v_add_u32_e32 v4, s19, v4
	v_ashrrev_i32_e32 v86, 8, v1
	v_bfe_u32 v82, v4, 7, 4
	v_mul_hi_i32_i24_e32 v89, 0x8a00, v86
	v_mul_i32_i24_e32 v88, 0x8a00, v86
	v_mul_u32_u24_e32 v82, 3, v82
	v_ashrrev_i32_e32 v87, 31, v86
	v_lshl_add_u64 v[88:89], s[86:87], 0, v[88:89]
	v_lshlrev_b32_e32 v82, 1, v82
	v_lshlrev_b64 v[98:99], 12, v[86:87]
	v_lshl_add_u64 v[86:87], v[88:89], 0, v[82:83]
	v_and_b32_e32 v80, 0x7f8, v4
	v_add_co_u32_e32 v102, vcc, s20, v86
	v_lshl_or_b32 v98, v80, 1, v98
	s_nop 0
	v_addc_co_u32_e32 v103, vcc, 0, v87, vcc
	v_lshl_add_u64 v[100:101], v[86:87], 0, s[16:17]
	v_lshl_add_u64 v[104:105], s[6:7], 0, v[98:99]
	v_lshl_add_u64 v[106:107], s[8:9], 0, v[98:99]
	v_lshl_add_u64 v[108:109], s[10:11], 0, v[98:99]
	global_load_dword v80, v[102:103], off offset:2112
	global_load_dwordx4 v[86:89], v[104:105], off
	global_load_ushort v82, v[100:101], off offset:4
	global_load_dwordx4 v[90:93], v[106:107], off
	global_load_dwordx4 v[94:97], v[108:109], off
	v_add_u32_e32 v1, s18, v1
	v_add_u32_e32 v4, s19, v4
	v_ashrrev_i32_e32 v126, 8, v1
	v_bfe_u32 v122, v4, 7, 4
	v_mul_hi_i32_i24_e32 v129, 0x8a00, v126
	v_mul_i32_i24_e32 v128, 0x8a00, v126
	v_mul_u32_u24_e32 v122, 3, v122
	v_ashrrev_i32_e32 v127, 31, v126
	v_lshl_add_u64 v[128:129], s[86:87], 0, v[128:129]
	v_lshlrev_b32_e32 v122, 1, v122
	v_lshlrev_b64 v[138:139], 12, v[126:127]
	v_lshl_add_u64 v[126:127], v[128:129], 0, v[122:123]
	v_and_b32_e32 v120, 0x7f8, v4
	v_add_co_u32_e32 v142, vcc, s20, v126
	v_lshl_or_b32 v138, v120, 1, v138
	s_nop 0
	v_addc_co_u32_e32 v143, vcc, 0, v127, vcc
	v_lshl_add_u64 v[140:141], v[126:127], 0, s[16:17]
	v_lshl_add_u64 v[144:145], s[6:7], 0, v[138:139]
	v_lshl_add_u64 v[146:147], s[8:9], 0, v[138:139]
	v_lshl_add_u64 v[148:149], s[10:11], 0, v[138:139]
	global_load_dword v120, v[142:143], off offset:2112
	global_load_dwordx4 v[126:129], v[144:145], off
	global_load_ushort v122, v[140:141], off offset:4
	global_load_dwordx4 v[130:133], v[146:147], off
	global_load_dwordx4 v[134:137], v[148:149], off
	v_add_u32_e32 v1, s18, v1
	v_cmp_lt_i32_e32 vcc, s23, v1
	v_add_u32_e32 v4, s19, v4
	s_or_b64 s[14:15], vcc, s[14:15]
	v_lshl_add_u64 v[18:19], s[12:13], 0, v[18:19]
	v_lshl_add_u64 v[58:59], s[12:13], 0, v[58:59]
	v_lshl_add_u64 v[98:99], s[12:13], 0, v[98:99]
	v_lshl_add_u64 v[138:139], s[12:13], 0, v[138:139]
	s_waitcnt vmcnt(19)
	v_lshlrev_b32_e32 v5, 16, v0
	v_and_b32_e32 v0, 0xffff0000, v0
	v_mul_f32_e32 v0, 0xbfb8aa3b, v0
	s_waitcnt vmcnt(17)
	v_lshlrev_b32_e32 v2, 16, v2
	v_mul_f32_e32 v5, 0xbfb8aa3b, v5
	v_exp_f32_e32 v0, v0
	v_mul_f32_e32 v2, 0xbfb8aa3b, v2
	v_exp_f32_e32 v5, v5
	v_exp_f32_e32 v2, v2
	v_add_f32_e32 v0, 1.0, v0
	v_rcp_f32_e32 v0, v0
	v_add_f32_e32 v5, 1.0, v5
	v_add_f32_e32 v32, 1.0, v2
	v_rcp_f32_e32 v2, v5
	v_rcp_f32_e32 v32, v32
	s_waitcnt vmcnt(16)
	v_lshlrev_b32_e32 v23, 16, v11
	v_lshlrev_b32_e32 v22, 16, v10
	v_and_b32_e32 v11, 0xffff0000, v11
	v_and_b32_e32 v10, 0xffff0000, v10
	v_lshlrev_b32_e32 v29, 16, v13
	v_lshlrev_b32_e32 v28, 16, v12
	v_and_b32_e32 v13, 0xffff0000, v13
	v_and_b32_e32 v12, 0xffff0000, v12
	v_lshlrev_b32_e32 v21, 16, v7
	v_lshlrev_b32_e32 v20, 16, v6
	v_and_b32_e32 v7, 0xffff0000, v7
	v_and_b32_e32 v6, 0xffff0000, v6
	v_lshlrev_b32_e32 v27, 16, v9
	v_lshlrev_b32_e32 v26, 16, v8
	v_and_b32_e32 v9, 0xffff0000, v9
	v_and_b32_e32 v8, 0xffff0000, v8
	v_pk_mul_f32 v[22:23], v[0:1], v[22:23] op_sel_hi:[0,1]
	v_pk_mul_f32 v[10:11], v[0:1], v[10:11] op_sel_hi:[0,1]
	v_pk_mul_f32 v[28:29], v[0:1], v[28:29] op_sel_hi:[0,1]
	v_pk_mul_f32 v[12:13], v[0:1], v[12:13] op_sel_hi:[0,1]
	s_waitcnt vmcnt(15)
	v_lshlrev_b32_e32 v25, 16, v15
	v_lshlrev_b32_e32 v24, 16, v14
	v_and_b32_e32 v15, 0xffff0000, v15
	v_and_b32_e32 v14, 0xffff0000, v14
	v_lshlrev_b32_e32 v31, 16, v17
	v_lshlrev_b32_e32 v30, 16, v16
	v_and_b32_e32 v17, 0xffff0000, v17
	v_and_b32_e32 v16, 0xffff0000, v16
	v_pk_fma_f32 v[20:21], v[2:3], v[20:21], v[22:23] op_sel_hi:[0,1,1]
	v_pk_fma_f32 v[6:7], v[2:3], v[6:7], v[10:11] op_sel_hi:[0,1,1]
	v_pk_fma_f32 v[10:11], v[2:3], v[26:27], v[28:29] op_sel_hi:[0,1,1]
	v_pk_fma_f32 v[8:9], v[2:3], v[8:9], v[12:13] op_sel_hi:[0,1,1]
	v_pk_fma_f32 v[12:13], v[32:33], v[24:25], v[20:21] op_sel_hi:[0,1,1]
	v_pk_fma_f32 v[6:7], v[32:33], v[14:15], v[6:7] op_sel_hi:[0,1,1]
	v_pk_fma_f32 v[10:11], v[32:33], v[30:31], v[10:11] op_sel_hi:[0,1,1]
	v_pk_fma_f32 v[8:9], v[32:33], v[16:17], v[8:9] op_sel_hi:[0,1,1]
	v_bfe_u32 v0, v9, 16, 1
	v_bfe_u32 v2, v8, 16, 1
	v_bfe_u32 v5, v7, 16, 1
	v_bfe_u32 v15, v12, 16, 1
	v_bfe_u32 v16, v13, 16, 1
	v_bfe_u32 v17, v10, 16, 1
	v_bfe_u32 v20, v11, 16, 1
	v_bfe_u32 v14, v6, 16, 1
	v_add3_u32 v5, v7, v5, s22
	v_add3_u32 v2, v8, v2, s22
	v_add3_u32 v0, v9, v0, s22
	v_add3_u32 v7, v11, v20, s22
	v_add3_u32 v8, v10, v17, s22
	v_add3_u32 v9, v13, v16, s22
	v_add3_u32 v10, v12, v15, s22
	v_add3_u32 v6, v6, v14, s22
	v_lshrrev_b32_e32 v10, 16, v10
	v_lshrrev_b32_e32 v11, 16, v9
	v_lshrrev_b32_e32 v8, 16, v8
	v_lshrrev_b32_e32 v7, 16, v7
	v_and_or_b32 v9, v0, s21, v7
	v_and_or_b32 v8, v2, s21, v8
	v_and_or_b32 v7, v5, s21, v11
	v_and_or_b32 v6, v6, s21, v10
	global_store_dwordx4 v[18:19], v[6:9], off
	s_waitcnt vmcnt(15)
	v_lshlrev_b32_e32 v45, 16, v40
	v_and_b32_e32 v40, 0xffff0000, v40
	v_mul_f32_e32 v40, 0xbfb8aa3b, v40
	s_waitcnt vmcnt(13)
	v_lshlrev_b32_e32 v42, 16, v42
	v_mul_f32_e32 v45, 0xbfb8aa3b, v45
	v_exp_f32_e32 v40, v40
	v_mul_f32_e32 v42, 0xbfb8aa3b, v42
	v_exp_f32_e32 v45, v45
	v_exp_f32_e32 v42, v42
	v_add_f32_e32 v40, 1.0, v40
	v_rcp_f32_e32 v40, v40
	v_add_f32_e32 v45, 1.0, v45
	v_add_f32_e32 v72, 1.0, v42
	v_rcp_f32_e32 v42, v45
	v_rcp_f32_e32 v72, v72
	s_waitcnt vmcnt(12)
	v_lshlrev_b32_e32 v63, 16, v51
	v_lshlrev_b32_e32 v62, 16, v50
	v_and_b32_e32 v51, 0xffff0000, v51
	v_and_b32_e32 v50, 0xffff0000, v50
	v_lshlrev_b32_e32 v69, 16, v53
	v_lshlrev_b32_e32 v68, 16, v52
	v_and_b32_e32 v53, 0xffff0000, v53
	v_and_b32_e32 v52, 0xffff0000, v52
	v_lshlrev_b32_e32 v61, 16, v47
	v_lshlrev_b32_e32 v60, 16, v46
	v_and_b32_e32 v47, 0xffff0000, v47
	v_and_b32_e32 v46, 0xffff0000, v46
	v_lshlrev_b32_e32 v67, 16, v49
	v_lshlrev_b32_e32 v66, 16, v48
	v_and_b32_e32 v49, 0xffff0000, v49
	v_and_b32_e32 v48, 0xffff0000, v48
	v_pk_mul_f32 v[62:63], v[40:41], v[62:63] op_sel_hi:[0,1]
	v_pk_mul_f32 v[50:51], v[40:41], v[50:51] op_sel_hi:[0,1]
	v_pk_mul_f32 v[68:69], v[40:41], v[68:69] op_sel_hi:[0,1]
	v_pk_mul_f32 v[52:53], v[40:41], v[52:53] op_sel_hi:[0,1]
	s_waitcnt vmcnt(11)
	v_lshlrev_b32_e32 v65, 16, v55
	v_lshlrev_b32_e32 v64, 16, v54
	v_and_b32_e32 v55, 0xffff0000, v55
	v_and_b32_e32 v54, 0xffff0000, v54
	v_lshlrev_b32_e32 v71, 16, v57
	v_lshlrev_b32_e32 v70, 16, v56
	v_and_b32_e32 v57, 0xffff0000, v57
	v_and_b32_e32 v56, 0xffff0000, v56
	v_pk_fma_f32 v[60:61], v[42:43], v[60:61], v[62:63] op_sel_hi:[0,1,1]
	v_pk_fma_f32 v[46:47], v[42:43], v[46:47], v[50:51] op_sel_hi:[0,1,1]
	v_pk_fma_f32 v[50:51], v[42:43], v[66:67], v[68:69] op_sel_hi:[0,1,1]
	v_pk_fma_f32 v[48:49], v[42:43], v[48:49], v[52:53] op_sel_hi:[0,1,1]
	v_pk_fma_f32 v[52:53], v[72:73], v[64:65], v[60:61] op_sel_hi:[0,1,1]
	v_pk_fma_f32 v[46:47], v[72:73], v[54:55], v[46:47] op_sel_hi:[0,1,1]
	v_pk_fma_f32 v[50:51], v[72:73], v[70:71], v[50:51] op_sel_hi:[0,1,1]
	v_pk_fma_f32 v[48:49], v[72:73], v[56:57], v[48:49] op_sel_hi:[0,1,1]
	v_bfe_u32 v40, v49, 16, 1
	v_bfe_u32 v42, v48, 16, 1
	v_bfe_u32 v45, v47, 16, 1
	v_bfe_u32 v55, v52, 16, 1
	v_bfe_u32 v56, v53, 16, 1
	v_bfe_u32 v57, v50, 16, 1
	v_bfe_u32 v60, v51, 16, 1
	v_bfe_u32 v54, v46, 16, 1
	v_add3_u32 v45, v47, v45, s22
	v_add3_u32 v42, v48, v42, s22
	v_add3_u32 v40, v49, v40, s22
	v_add3_u32 v47, v51, v60, s22
	v_add3_u32 v48, v50, v57, s22
	v_add3_u32 v49, v53, v56, s22
	v_add3_u32 v50, v52, v55, s22
	v_add3_u32 v46, v46, v54, s22
	v_lshrrev_b32_e32 v50, 16, v50
	v_lshrrev_b32_e32 v51, 16, v49
	v_lshrrev_b32_e32 v48, 16, v48
	v_lshrrev_b32_e32 v47, 16, v47
	v_and_or_b32 v49, v40, s21, v47
	v_and_or_b32 v48, v42, s21, v48
	v_and_or_b32 v47, v45, s21, v51
	v_and_or_b32 v46, v46, s21, v50
	global_store_dwordx4 v[58:59], v[46:49], off
	s_waitcnt vmcnt(11)
	v_lshlrev_b32_e32 v85, 16, v80
	v_and_b32_e32 v80, 0xffff0000, v80
	v_mul_f32_e32 v80, 0xbfb8aa3b, v80
	s_waitcnt vmcnt(9)
	v_lshlrev_b32_e32 v82, 16, v82
	v_mul_f32_e32 v85, 0xbfb8aa3b, v85
	v_exp_f32_e32 v80, v80
	v_mul_f32_e32 v82, 0xbfb8aa3b, v82
	v_exp_f32_e32 v85, v85
	v_exp_f32_e32 v82, v82
	v_add_f32_e32 v80, 1.0, v80
	v_rcp_f32_e32 v80, v80
	v_add_f32_e32 v85, 1.0, v85
	v_add_f32_e32 v112, 1.0, v82
	v_rcp_f32_e32 v82, v85
	v_rcp_f32_e32 v112, v112
	s_waitcnt vmcnt(8)
	v_lshlrev_b32_e32 v103, 16, v91
	v_lshlrev_b32_e32 v102, 16, v90
	v_and_b32_e32 v91, 0xffff0000, v91
	v_and_b32_e32 v90, 0xffff0000, v90
	v_lshlrev_b32_e32 v109, 16, v93
	v_lshlrev_b32_e32 v108, 16, v92
	v_and_b32_e32 v93, 0xffff0000, v93
	v_and_b32_e32 v92, 0xffff0000, v92
	v_lshlrev_b32_e32 v101, 16, v87
	v_lshlrev_b32_e32 v100, 16, v86
	v_and_b32_e32 v87, 0xffff0000, v87
	v_and_b32_e32 v86, 0xffff0000, v86
	v_lshlrev_b32_e32 v107, 16, v89
	v_lshlrev_b32_e32 v106, 16, v88
	v_and_b32_e32 v89, 0xffff0000, v89
	v_and_b32_e32 v88, 0xffff0000, v88
	v_pk_mul_f32 v[102:103], v[80:81], v[102:103] op_sel_hi:[0,1]
	v_pk_mul_f32 v[90:91], v[80:81], v[90:91] op_sel_hi:[0,1]
	v_pk_mul_f32 v[108:109], v[80:81], v[108:109] op_sel_hi:[0,1]
	v_pk_mul_f32 v[92:93], v[80:81], v[92:93] op_sel_hi:[0,1]
	s_waitcnt vmcnt(7)
	v_lshlrev_b32_e32 v105, 16, v95
	v_lshlrev_b32_e32 v104, 16, v94
	v_and_b32_e32 v95, 0xffff0000, v95
	v_and_b32_e32 v94, 0xffff0000, v94
	v_lshlrev_b32_e32 v111, 16, v97
	v_lshlrev_b32_e32 v110, 16, v96
	v_and_b32_e32 v97, 0xffff0000, v97
	v_and_b32_e32 v96, 0xffff0000, v96
	v_pk_fma_f32 v[100:101], v[82:83], v[100:101], v[102:103] op_sel_hi:[0,1,1]
	v_pk_fma_f32 v[86:87], v[82:83], v[86:87], v[90:91] op_sel_hi:[0,1,1]
	v_pk_fma_f32 v[90:91], v[82:83], v[106:107], v[108:109] op_sel_hi:[0,1,1]
	v_pk_fma_f32 v[88:89], v[82:83], v[88:89], v[92:93] op_sel_hi:[0,1,1]
	v_pk_fma_f32 v[92:93], v[112:113], v[104:105], v[100:101] op_sel_hi:[0,1,1]
	v_pk_fma_f32 v[86:87], v[112:113], v[94:95], v[86:87] op_sel_hi:[0,1,1]
	v_pk_fma_f32 v[90:91], v[112:113], v[110:111], v[90:91] op_sel_hi:[0,1,1]
	v_pk_fma_f32 v[88:89], v[112:113], v[96:97], v[88:89] op_sel_hi:[0,1,1]
	v_bfe_u32 v80, v89, 16, 1
	v_bfe_u32 v82, v88, 16, 1
	v_bfe_u32 v85, v87, 16, 1
	v_bfe_u32 v95, v92, 16, 1
	v_bfe_u32 v96, v93, 16, 1
	v_bfe_u32 v97, v90, 16, 1
	v_bfe_u32 v100, v91, 16, 1
	v_bfe_u32 v94, v86, 16, 1
	v_add3_u32 v85, v87, v85, s22
	v_add3_u32 v82, v88, v82, s22
	v_add3_u32 v80, v89, v80, s22
	v_add3_u32 v87, v91, v100, s22
	v_add3_u32 v88, v90, v97, s22
	v_add3_u32 v89, v93, v96, s22
	v_add3_u32 v90, v92, v95, s22
	v_add3_u32 v86, v86, v94, s22
	v_lshrrev_b32_e32 v90, 16, v90
	v_lshrrev_b32_e32 v91, 16, v89
	v_lshrrev_b32_e32 v88, 16, v88
	v_lshrrev_b32_e32 v87, 16, v87
	v_and_or_b32 v89, v80, s21, v87
	v_and_or_b32 v88, v82, s21, v88
	v_and_or_b32 v87, v85, s21, v91
	v_and_or_b32 v86, v86, s21, v90
	global_store_dwordx4 v[98:99], v[86:89], off
	s_waitcnt vmcnt(7)
	v_lshlrev_b32_e32 v125, 16, v120
	v_and_b32_e32 v120, 0xffff0000, v120
	v_mul_f32_e32 v120, 0xbfb8aa3b, v120
	s_waitcnt vmcnt(5)
	v_lshlrev_b32_e32 v122, 16, v122
	v_mul_f32_e32 v125, 0xbfb8aa3b, v125
	v_exp_f32_e32 v120, v120
	v_mul_f32_e32 v122, 0xbfb8aa3b, v122
	v_exp_f32_e32 v125, v125
	v_exp_f32_e32 v122, v122
	v_add_f32_e32 v120, 1.0, v120
	v_rcp_f32_e32 v120, v120
	v_add_f32_e32 v125, 1.0, v125
	v_add_f32_e32 v152, 1.0, v122
	v_rcp_f32_e32 v122, v125
	v_rcp_f32_e32 v152, v152
	s_waitcnt vmcnt(4)
	v_lshlrev_b32_e32 v143, 16, v131
	v_lshlrev_b32_e32 v142, 16, v130
	v_and_b32_e32 v131, 0xffff0000, v131
	v_and_b32_e32 v130, 0xffff0000, v130
	v_lshlrev_b32_e32 v149, 16, v133
	v_lshlrev_b32_e32 v148, 16, v132
	v_and_b32_e32 v133, 0xffff0000, v133
	v_and_b32_e32 v132, 0xffff0000, v132
	v_lshlrev_b32_e32 v141, 16, v127
	v_lshlrev_b32_e32 v140, 16, v126
	v_and_b32_e32 v127, 0xffff0000, v127
	v_and_b32_e32 v126, 0xffff0000, v126
	v_lshlrev_b32_e32 v147, 16, v129
	v_lshlrev_b32_e32 v146, 16, v128
	v_and_b32_e32 v129, 0xffff0000, v129
	v_and_b32_e32 v128, 0xffff0000, v128
	v_pk_mul_f32 v[142:143], v[120:121], v[142:143] op_sel_hi:[0,1]
	v_pk_mul_f32 v[130:131], v[120:121], v[130:131] op_sel_hi:[0,1]
	v_pk_mul_f32 v[148:149], v[120:121], v[148:149] op_sel_hi:[0,1]
	v_pk_mul_f32 v[132:133], v[120:121], v[132:133] op_sel_hi:[0,1]
	s_waitcnt vmcnt(3)
	v_lshlrev_b32_e32 v145, 16, v135
	v_lshlrev_b32_e32 v144, 16, v134
	v_and_b32_e32 v135, 0xffff0000, v135
	v_and_b32_e32 v134, 0xffff0000, v134
	v_lshlrev_b32_e32 v151, 16, v137
	v_lshlrev_b32_e32 v150, 16, v136
	v_and_b32_e32 v137, 0xffff0000, v137
	v_and_b32_e32 v136, 0xffff0000, v136
	v_pk_fma_f32 v[140:141], v[122:123], v[140:141], v[142:143] op_sel_hi:[0,1,1]
	v_pk_fma_f32 v[126:127], v[122:123], v[126:127], v[130:131] op_sel_hi:[0,1,1]
	v_pk_fma_f32 v[130:131], v[122:123], v[146:147], v[148:149] op_sel_hi:[0,1,1]
	v_pk_fma_f32 v[128:129], v[122:123], v[128:129], v[132:133] op_sel_hi:[0,1,1]
	v_pk_fma_f32 v[132:133], v[152:153], v[144:145], v[140:141] op_sel_hi:[0,1,1]
	v_pk_fma_f32 v[126:127], v[152:153], v[134:135], v[126:127] op_sel_hi:[0,1,1]
	v_pk_fma_f32 v[130:131], v[152:153], v[150:151], v[130:131] op_sel_hi:[0,1,1]
	v_pk_fma_f32 v[128:129], v[152:153], v[136:137], v[128:129] op_sel_hi:[0,1,1]
	v_bfe_u32 v120, v129, 16, 1
	v_bfe_u32 v122, v128, 16, 1
	v_bfe_u32 v125, v127, 16, 1
	v_bfe_u32 v135, v132, 16, 1
	v_bfe_u32 v136, v133, 16, 1
	v_bfe_u32 v137, v130, 16, 1
	v_bfe_u32 v140, v131, 16, 1
	v_bfe_u32 v134, v126, 16, 1
	v_add3_u32 v125, v127, v125, s22
	v_add3_u32 v122, v128, v122, s22
	v_add3_u32 v120, v129, v120, s22
	v_add3_u32 v127, v131, v140, s22
	v_add3_u32 v128, v130, v137, s22
	v_add3_u32 v129, v133, v136, s22
	v_add3_u32 v130, v132, v135, s22
	v_add3_u32 v126, v126, v134, s22
	v_lshrrev_b32_e32 v130, 16, v130
	v_lshrrev_b32_e32 v131, 16, v129
	v_lshrrev_b32_e32 v128, 16, v128
	v_lshrrev_b32_e32 v127, 16, v127
	v_and_or_b32 v129, v120, s21, v127
	v_and_or_b32 v128, v122, s21, v128
	v_and_or_b32 v127, v125, s21, v131
	v_and_or_b32 v126, v126, s21, v130
	global_store_dwordx4 v[138:139], v[126:129], off
	s_andn2_b64 exec, exec, s[14:15]
	s_cbranch_execnz .LBB0_1060
	s_branch .LBB0_1061
